# norm+router phase: router bias loaded with the prologue loads instead of a separate round trip after the x loop
# baseline (speedup 1.0000x reference)
.LBB0_776:
	s_waitcnt lgkmcnt(0)
	s_barrier
	s_and_saveexec_b64 s[0:1], s[42:43]
	ds_write_b32 v60, v2
	s_or_b64 exec, exec, s[0:1]
	s_add_i32 s0, s18, s2
	s_lshl_b32 s21, s0, 4
	s_cmpk_lt_i32 s0, 0x800
	s_cselect_b64 s[14:15], -1, 0
	s_and_b64 s[0:1], s[14:15], exec
	s_cselect_b32 s3, s21, 0
	s_lshl_b32 s0, s2, 4
	v_readlane_b32 s1, v251, 58
	s_add_i32 s0, s0, s1
	s_ashr_i32 s0, s0, 14
	s_min_i32 s0, s0, 1
	s_add_i32 s0, s0, s19
	v_mad_i64_i32 v[4:5], s[0:1], s0, v223, v[40:41]
	s_movk_i32 s0, 0x4000
	s_nop 0
	v_add_co_u32_e32 v6, vcc, s0, v4
	s_movk_i32 s0, 0x3000
	s_nop 0
	v_addc_co_u32_e32 v7, vcc, 0, v5, vcc
	v_add_co_u32_e32 v4, vcc, s0, v4
	v_or_b32_e32 v8, s3, v3
	s_nop 0
	v_addc_co_u32_e32 v5, vcc, 0, v5, vcc
	global_load_dword v10, v[6:7], off
	s_nop 0
	global_load_dword v6, v[6:7], off offset:2048
	s_nop 0
	global_load_dword v7, v[4:5], off
	global_load_dword v11, v[4:5], off offset:2048
	global_load_dword v12, v[36:37], off
	global_load_dword v13, v[38:39], off offset:2048
	v_ashrrev_i32_e32 v9, 31, v8
	v_lshlrev_b64 v[4:5], 6, v[8:9]
	v_lshl_add_u64 v[4:5], v[32:33], 0, v[4:5]
	global_load_dwordx4 v[152:155], v2, s[6:7] offset:48
	global_load_dwordx4 v[156:159], v2, s[6:7] offset:32
	global_load_dwordx4 v[160:163], v2, s[6:7] offset:16
	global_load_dwordx4 v[164:167], v2, s[6:7]
	global_load_dwordx4 v[146:149], v[4:5], off
	v_lshlrev_b64 v[150:151], 11, v[8:9]
	v_lshl_add_u64 v[144:145], v[44:45], 0, v[150:151]
	v_lshl_add_u64 v[144:145], s[8:9], 0, v[144:145]
	v_add_co_u32_e32 v144, vcc, 0x26600000, v144
	s_nop 1
	v_addc_co_u32_e32 v145, vcc, 0, v145, vcc
	s_nop 0
	global_load_dwordx4 v[112:115], v[144:145], off
	global_load_dwordx4 v[116:119], v[144:145], off offset:64
	global_load_dwordx4 v[120:123], v[144:145], off offset:128
	global_load_dwordx4 v[124:127], v[144:145], off offset:192
	global_load_dwordx4 v[128:131], v[144:145], off offset:256
	global_load_dwordx4 v[132:135], v[144:145], off offset:320
	global_load_dwordx4 v[136:139], v[144:145], off offset:384
	global_load_dwordx4 v[140:143], v[144:145], off offset:448
	s_mov_b32 s0, -8
	v_mov_b32_e32 v65, v58
	v_mov_b32_e32 v66, v62
	s_waitcnt vmcnt(18)
	v_add_f32_e32 v10, 1.0, v10
	s_waitcnt vmcnt(17)
	v_add_f32_e32 v6, 1.0, v6
	s_waitcnt vmcnt(15)
	ds_write2st64_b32 v59, v7, v11 offset0:145 offset1:153
	s_waitcnt vmcnt(14)
	v_mul_f32_e32 v7, v12, v10
	s_waitcnt vmcnt(13)
	v_mul_f32_e32 v6, v13, v6
	ds_write2st64_b32 v59, v7, v6 offset0:129 offset1:137
	s_waitcnt lgkmcnt(0)
	s_barrier
	s_waitcnt vmcnt(8)
	v_mov_b32_e32 v4, v146
	v_mov_b32_e32 v5, v147
	v_mov_b32_e32 v6, v148
	v_mov_b32_e32 v7, v149
	v_mov_b32_e32 v10, v5
	v_mov_b32_e32 v11, v6
	v_mov_b32_e32 v5, v7
	v_pk_add_f32 v[4:5], v[10:11], v[4:5]
	v_lshlrev_b64 v[10:11], 10, v[8:9]
	v_add_f32_e32 v5, v4, v5
	ds_bpermute_b32 v6, v56, v5
	v_mov_b32_e32 v4, 0
	v_lshlrev_b64 v[8:9], 11, v[8:9]
	v_lshl_add_u64 v[48:49], v[44:45], 0, v[8:9]
	v_lshl_add_u64 v[50:51], v[34:35], 0, v[10:11]
	s_waitcnt lgkmcnt(0)
	v_add_f32_e32 v7, v5, v6
	ds_bpermute_b32 v12, v57, v7
	v_mov_b32_e32 v5, v4
	v_mov_b32_e32 v6, v4
	s_waitcnt lgkmcnt(0)
	v_add_f32_e32 v7, v7, v12
	v_fmamk_f32 v7, v7, 0x3a800000, v210
	v_rsq_f32_e32 v46, v7
	v_mov_b32_e32 v7, v4
	v_mov_b32_e32 v47, v46
	v_mov_b32_e32 v52, v46
	v_mov_b32_e32 v53, v46
	s_waitcnt vmcnt(0)

.LPF_skip:
	v_lshlrev_b32_e32 v54, 16, v68
	v_and_b32_e32 v55, 0xffff0000, v68
	v_lshlrev_b32_e32 v88, 16, v69
	v_and_b32_e32 v89, 0xffff0000, v69
	v_lshlrev_b32_e32 v90, 16, v70
	v_and_b32_e32 v91, 0xffff0000, v70
	v_lshlrev_b32_e32 v92, 16, v71
	v_and_b32_e32 v93, 0xffff0000, v71
	ds_read_b128 v[68:71], v66
	ds_read_b128 v[76:79], v66 offset:16
	ds_read_b128 v[80:83], v66 offset:4096
	ds_read_b128 v[84:87], v66 offset:4112
	v_pk_mul_f32 v[54:55], v[46:47], v[54:55]
	v_pk_mul_f32 v[88:89], v[52:53], v[88:89]
	s_waitcnt lgkmcnt(1)
	v_pk_fma_f32 v[54:55], v[54:55], v[68:69], v[80:81]
	v_pk_mul_f32 v[68:69], v[46:47], v[90:91]
	v_mov_b32_e32 v80, v2
	s_waitcnt lgkmcnt(0)
	v_pk_fma_f32 v[76:77], v[68:69], v[76:77], v[84:85]
	v_mov_b32_e32 v81, v2
	v_cvt_pk_fp8_f32 v80, v54, v55
	v_cvt_pk_fp8_f32 v81, v76, v77
	v_pk_fma_f32 v[82:83], v[88:89], v[70:71], v[82:83]
	v_pk_mul_f32 v[70:71], v[52:53], v[92:93]
	v_cvt_pk_bf16_f32 v68, v54, v55
	v_pk_fma_f32 v[78:79], v[70:71], v[78:79], v[86:87]
	v_cvt_pk_bf16_f32 v69, v82, v83
	v_cvt_pk_bf16_f32 v70, v76, v77
	v_cvt_pk_bf16_f32 v71, v78, v79
	v_cvt_pk_fp8_f32 v80, v82, v83 op_sel:[0,0,1]
	v_cvt_pk_fp8_f32 v81, v78, v79 op_sel:[0,0,1]
	ds_read_b128 v[76:79], v65
	v_lshl_add_u64 v[54:55], s[8:9], 0, v[50:51]
	v_add_co_u32_e32 v54, vcc, s1, v54
	s_waitcnt lgkmcnt(0)
	v_mfma_f32_16x16x32_bf16 v[4:7], v[68:71], v[76:79], v[4:7]
	v_addc_co_u32_e32 v55, vcc, 0, v55, vcc
	global_store_dwordx2 v[54:55], v[80:81], off
	v_lshlrev_b32_e32 v84, 16, v72
	v_and_b32_e32 v85, 0xffff0000, v72
	v_lshlrev_b32_e32 v86, 16, v73
	v_and_b32_e32 v87, 0xffff0000, v73
	v_lshlrev_b32_e32 v88, 16, v74
	v_and_b32_e32 v89, 0xffff0000, v74
	v_lshlrev_b32_e32 v90, 16, v75
	v_and_b32_e32 v91, 0xffff0000, v75
	ds_read_b128 v[68:71], v66 offset:128
	ds_read_b128 v[72:75], v66 offset:144
	ds_read_b128 v[76:79], v66 offset:4224
	ds_read_b128 v[80:83], v66 offset:4240
	v_pk_mul_f32 v[84:85], v[46:47], v[84:85]
	v_pk_mul_f32 v[86:87], v[52:53], v[86:87]
	v_lshl_add_u64 v[50:51], v[50:51], 0, s[2:3]
	s_waitcnt lgkmcnt(1)
	v_pk_fma_f32 v[76:77], v[84:85], v[68:69], v[76:77]
	v_pk_mul_f32 v[68:69], v[46:47], v[88:89]
	v_pk_fma_f32 v[78:79], v[86:87], v[70:71], v[78:79]
	s_waitcnt lgkmcnt(0)
	v_pk_fma_f32 v[72:73], v[68:69], v[72:73], v[80:81]
	v_mov_b32_e32 v80, v2
	v_mov_b32_e32 v81, v2
	v_cvt_pk_fp8_f32 v80, v76, v77
	v_cvt_pk_fp8_f32 v81, v72, v73
	v_pk_mul_f32 v[70:71], v[52:53], v[90:91]
	v_cvt_pk_bf16_f32 v68, v76, v77
	v_pk_fma_f32 v[74:75], v[70:71], v[74:75], v[82:83]
	v_cvt_pk_bf16_f32 v69, v78, v79
	v_cvt_pk_bf16_f32 v70, v72, v73
	v_cvt_pk_bf16_f32 v71, v74, v75
	v_cvt_pk_fp8_f32 v80, v78, v79 op_sel:[0,0,1]
	v_cvt_pk_fp8_f32 v81, v74, v75 op_sel:[0,0,1]
	ds_read_b128 v[72:75], v65 offset:64
	s_waitcnt lgkmcnt(0)
	v_mfma_f32_16x16x32_bf16 v[4:7], v[68:71], v[72:75], v[4:7]
	global_store_dwordx2 v[54:55], v[80:81], off offset:32
	v_lshlrev_b32_e32 v80, 16, v28
	v_and_b32_e32 v81, 0xffff0000, v28
	v_lshlrev_b32_e32 v82, 16, v29
	v_and_b32_e32 v83, 0xffff0000, v29
	v_lshlrev_b32_e32 v84, 16, v30
	v_and_b32_e32 v85, 0xffff0000, v30
	v_lshlrev_b32_e32 v86, 16, v31
	v_and_b32_e32 v87, 0xffff0000, v31
	ds_read_b128 v[28:31], v66 offset:256
	ds_read_b128 v[68:71], v66 offset:272
	ds_read_b128 v[72:75], v66 offset:4352
	ds_read_b128 v[76:79], v66 offset:4368
	v_pk_mul_f32 v[80:81], v[46:47], v[80:81]
	v_pk_mul_f32 v[82:83], v[52:53], v[82:83]
	s_waitcnt lgkmcnt(1)
	v_pk_fma_f32 v[72:73], v[80:81], v[28:29], v[72:73]
	v_pk_mul_f32 v[28:29], v[46:47], v[84:85]
	v_pk_fma_f32 v[74:75], v[82:83], v[30:31], v[74:75]
	s_waitcnt lgkmcnt(0)
	v_pk_fma_f32 v[68:69], v[28:29], v[68:69], v[76:77]
	v_mov_b32_e32 v76, v2
	v_mov_b32_e32 v77, v2
	v_cvt_pk_fp8_f32 v76, v72, v73
	v_cvt_pk_fp8_f32 v77, v68, v69
	v_pk_mul_f32 v[30:31], v[52:53], v[86:87]
	v_cvt_pk_bf16_f32 v28, v72, v73
	v_pk_fma_f32 v[70:71], v[30:31], v[70:71], v[78:79]
	v_cvt_pk_bf16_f32 v29, v74, v75
	v_cvt_pk_bf16_f32 v30, v68, v69
	v_cvt_pk_bf16_f32 v31, v70, v71
	v_cvt_pk_fp8_f32 v76, v74, v75 op_sel:[0,0,1]
	v_cvt_pk_fp8_f32 v77, v70, v71 op_sel:[0,0,1]
	ds_read_b128 v[68:71], v65 offset:128
	s_waitcnt lgkmcnt(0)
	v_mfma_f32_16x16x32_bf16 v[4:7], v[28:31], v[68:71], v[4:7]
	global_store_dwordx2 v[54:55], v[76:77], off offset:64
	v_lshlrev_b32_e32 v76, 16, v24
	v_and_b32_e32 v77, 0xffff0000, v24
	v_lshlrev_b32_e32 v78, 16, v25
	v_and_b32_e32 v79, 0xffff0000, v25
	v_lshlrev_b32_e32 v80, 16, v26
	v_and_b32_e32 v81, 0xffff0000, v26
	v_lshlrev_b32_e32 v82, 16, v27
	v_and_b32_e32 v83, 0xffff0000, v27
	ds_read_b128 v[24:27], v66 offset:384
	ds_read_b128 v[28:31], v66 offset:400
	ds_read_b128 v[68:71], v66 offset:4480
	ds_read_b128 v[72:75], v66 offset:4496
	v_pk_mul_f32 v[76:77], v[46:47], v[76:77]
	v_pk_mul_f32 v[78:79], v[52:53], v[78:79]
	s_waitcnt lgkmcnt(1)
	v_pk_fma_f32 v[68:69], v[76:77], v[24:25], v[68:69]
	v_pk_mul_f32 v[24:25], v[46:47], v[80:81]
	v_pk_fma_f32 v[70:71], v[78:79], v[26:27], v[70:71]
	s_waitcnt lgkmcnt(0)
	v_pk_fma_f32 v[28:29], v[24:25], v[28:29], v[72:73]
	v_mov_b32_e32 v72, v2
	v_mov_b32_e32 v73, v2
	v_cvt_pk_fp8_f32 v72, v68, v69
	v_cvt_pk_fp8_f32 v73, v28, v29
	v_pk_mul_f32 v[26:27], v[52:53], v[82:83]
	v_cvt_pk_bf16_f32 v24, v68, v69
	v_pk_fma_f32 v[30:31], v[26:27], v[30:31], v[74:75]
	v_cvt_pk_bf16_f32 v25, v70, v71
	v_cvt_pk_bf16_f32 v26, v28, v29
	v_cvt_pk_bf16_f32 v27, v30, v31
	v_cvt_pk_fp8_f32 v72, v70, v71 op_sel:[0,0,1]
	v_cvt_pk_fp8_f32 v73, v30, v31 op_sel:[0,0,1]
	ds_read_b128 v[28:31], v65 offset:192
	s_waitcnt lgkmcnt(0)
	v_mfma_f32_16x16x32_bf16 v[4:7], v[24:27], v[28:31], v[4:7]
	global_store_dwordx2 v[54:55], v[72:73], off offset:96
	v_lshlrev_b32_e32 v72, 16, v20
	v_and_b32_e32 v73, 0xffff0000, v20
	v_lshlrev_b32_e32 v74, 16, v21
	v_and_b32_e32 v75, 0xffff0000, v21
	v_lshlrev_b32_e32 v76, 16, v22
	v_and_b32_e32 v77, 0xffff0000, v22
	v_lshlrev_b32_e32 v78, 16, v23
	v_and_b32_e32 v79, 0xffff0000, v23
	ds_read_b128 v[20:23], v66 offset:512
	ds_read_b128 v[24:27], v66 offset:528
	ds_read_b128 v[28:31], v66 offset:4608
	ds_read_b128 v[68:71], v66 offset:4624
	v_pk_mul_f32 v[72:73], v[46:47], v[72:73]
	v_pk_mul_f32 v[74:75], v[52:53], v[74:75]
	s_waitcnt lgkmcnt(1)
	v_pk_fma_f32 v[28:29], v[72:73], v[20:21], v[28:29]
	v_pk_mul_f32 v[20:21], v[46:47], v[76:77]
	v_pk_fma_f32 v[30:31], v[74:75], v[22:23], v[30:31]
	s_waitcnt lgkmcnt(0)
	v_pk_fma_f32 v[24:25], v[20:21], v[24:25], v[68:69]
	v_mov_b32_e32 v68, v2
	v_mov_b32_e32 v69, v2
	v_cvt_pk_fp8_f32 v68, v28, v29
	v_cvt_pk_fp8_f32 v69, v24, v25
	v_pk_mul_f32 v[22:23], v[52:53], v[78:79]
	v_cvt_pk_bf16_f32 v20, v28, v29
	v_pk_fma_f32 v[26:27], v[22:23], v[26:27], v[70:71]
	v_cvt_pk_bf16_f32 v21, v30, v31
	v_cvt_pk_bf16_f32 v22, v24, v25
	v_cvt_pk_bf16_f32 v23, v26, v27
	v_cvt_pk_fp8_f32 v68, v30, v31 op_sel:[0,0,1]
	v_cvt_pk_fp8_f32 v69, v26, v27 op_sel:[0,0,1]
	ds_read_b128 v[24:27], v65 offset:256
	s_waitcnt lgkmcnt(0)
	v_mfma_f32_16x16x32_bf16 v[4:7], v[20:23], v[24:27], v[4:7]
	global_store_dwordx2 v[54:55], v[68:69], off offset:128
	v_lshlrev_b32_e32 v68, 16, v16
	v_and_b32_e32 v69, 0xffff0000, v16
	v_lshlrev_b32_e32 v70, 16, v17
	v_and_b32_e32 v71, 0xffff0000, v17
	v_lshlrev_b32_e32 v72, 16, v18
	v_and_b32_e32 v73, 0xffff0000, v18
	v_lshlrev_b32_e32 v74, 16, v19
	v_and_b32_e32 v75, 0xffff0000, v19
	ds_read_b128 v[16:19], v66 offset:640
	ds_read_b128 v[20:23], v66 offset:656
	ds_read_b128 v[24:27], v66 offset:4736
	ds_read_b128 v[28:31], v66 offset:4752
	v_pk_mul_f32 v[68:69], v[46:47], v[68:69]
	v_pk_mul_f32 v[70:71], v[52:53], v[70:71]
	s_waitcnt lgkmcnt(1)
	v_pk_fma_f32 v[24:25], v[68:69], v[16:17], v[24:25]
	v_pk_mul_f32 v[16:17], v[46:47], v[72:73]
	v_pk_fma_f32 v[26:27], v[70:71], v[18:19], v[26:27]
	s_waitcnt lgkmcnt(0)
	v_pk_fma_f32 v[20:21], v[16:17], v[20:21], v[28:29]
	v_mov_b32_e32 v28, v2
	v_mov_b32_e32 v29, v2
	v_cvt_pk_fp8_f32 v28, v24, v25
	v_cvt_pk_fp8_f32 v29, v20, v21
	v_pk_mul_f32 v[18:19], v[52:53], v[74:75]
	v_cvt_pk_bf16_f32 v16, v24, v25
	v_pk_fma_f32 v[22:23], v[18:19], v[22:23], v[30:31]
	v_cvt_pk_bf16_f32 v17, v26, v27
	v_cvt_pk_bf16_f32 v18, v20, v21
	v_cvt_pk_bf16_f32 v19, v22, v23
	v_cvt_pk_fp8_f32 v28, v26, v27 op_sel:[0,0,1]
	v_cvt_pk_fp8_f32 v29, v22, v23 op_sel:[0,0,1]
	ds_read_b128 v[20:23], v65 offset:320
	s_waitcnt lgkmcnt(0)
	v_mfma_f32_16x16x32_bf16 v[4:7], v[16:19], v[20:23], v[4:7]
	global_store_dwordx2 v[54:55], v[28:29], off offset:160
	v_lshlrev_b32_e32 v28, 16, v12
	v_and_b32_e32 v29, 0xffff0000, v12
	v_lshlrev_b32_e32 v30, 16, v13
	v_and_b32_e32 v31, 0xffff0000, v13
	v_lshlrev_b32_e32 v68, 16, v14
	v_and_b32_e32 v69, 0xffff0000, v14
	v_lshlrev_b32_e32 v70, 16, v15
	v_and_b32_e32 v71, 0xffff0000, v15
	ds_read_b128 v[12:15], v66 offset:768
	ds_read_b128 v[16:19], v66 offset:784
	ds_read_b128 v[20:23], v66 offset:4864
	ds_read_b128 v[24:27], v66 offset:4880
	v_pk_mul_f32 v[28:29], v[46:47], v[28:29]
	v_pk_mul_f32 v[30:31], v[52:53], v[30:31]
	s_waitcnt lgkmcnt(1)
	v_pk_fma_f32 v[20:21], v[28:29], v[12:13], v[20:21]
	v_pk_mul_f32 v[12:13], v[46:47], v[68:69]
	v_pk_fma_f32 v[22:23], v[30:31], v[14:15], v[22:23]
	s_waitcnt lgkmcnt(0)
	v_pk_fma_f32 v[16:17], v[12:13], v[16:17], v[24:25]
	v_mov_b32_e32 v24, v2
	v_mov_b32_e32 v25, v2
	v_cvt_pk_fp8_f32 v24, v20, v21
	v_cvt_pk_fp8_f32 v25, v16, v17
	v_pk_mul_f32 v[14:15], v[52:53], v[70:71]
	v_cvt_pk_bf16_f32 v12, v20, v21
	v_pk_fma_f32 v[18:19], v[14:15], v[18:19], v[26:27]
	v_cvt_pk_bf16_f32 v13, v22, v23
	v_cvt_pk_bf16_f32 v14, v16, v17
	v_cvt_pk_bf16_f32 v15, v18, v19
	v_cvt_pk_fp8_f32 v24, v22, v23 op_sel:[0,0,1]
	v_cvt_pk_fp8_f32 v25, v18, v19 op_sel:[0,0,1]
	ds_read_b128 v[16:19], v65 offset:384
	s_waitcnt lgkmcnt(0)
	v_mfma_f32_16x16x32_bf16 v[4:7], v[12:15], v[16:19], v[4:7]
	global_store_dwordx2 v[54:55], v[24:25], off offset:192
	v_lshlrev_b32_e32 v24, 16, v8
	v_and_b32_e32 v25, 0xffff0000, v8
	v_lshlrev_b32_e32 v26, 16, v9
	v_and_b32_e32 v27, 0xffff0000, v9
	v_lshlrev_b32_e32 v28, 16, v10
	v_and_b32_e32 v29, 0xffff0000, v10
	v_lshlrev_b32_e32 v30, 16, v11
	v_and_b32_e32 v31, 0xffff0000, v11
	ds_read_b128 v[8:11], v66 offset:896
	ds_read_b128 v[12:15], v66 offset:912
	ds_read_b128 v[16:19], v66 offset:4992
	ds_read_b128 v[20:23], v66 offset:5008
	v_pk_mul_f32 v[24:25], v[46:47], v[24:25]
	v_pk_mul_f32 v[26:27], v[52:53], v[26:27]
	v_add_u32_e32 v66, 0x400, v66
	s_waitcnt lgkmcnt(1)
	v_pk_fma_f32 v[16:17], v[24:25], v[8:9], v[16:17]
	v_pk_mul_f32 v[8:9], v[46:47], v[28:29]
	v_pk_fma_f32 v[18:19], v[26:27], v[10:11], v[18:19]
	s_waitcnt lgkmcnt(0)
	v_pk_fma_f32 v[12:13], v[8:9], v[12:13], v[20:21]
	v_mov_b32_e32 v21, v2
	v_cvt_pk_fp8_f32 v21, v12, v13
	v_pk_mul_f32 v[10:11], v[52:53], v[30:31]
	v_cvt_pk_bf16_f32 v8, v16, v17
	v_pk_fma_f32 v[14:15], v[10:11], v[14:15], v[22:23]
	v_cvt_pk_bf16_f32 v9, v18, v19
	v_cvt_pk_bf16_f32 v10, v12, v13
	v_cvt_pk_bf16_f32 v11, v14, v15
	v_mov_b32_e32 v20, v2
	v_cvt_pk_fp8_f32 v21, v14, v15 op_sel:[0,0,1]
	ds_read_b128 v[12:15], v65 offset:448
	v_cvt_pk_fp8_f32 v20, v16, v17
	s_waitcnt lgkmcnt(0)
	v_mfma_f32_16x16x32_bf16 v[4:7], v[8:11], v[12:15], v[4:7]
	v_cvt_pk_fp8_f32 v20, v18, v19 op_sel:[0,0,1]
	v_add_u32_e32 v65, 0x200, v65
	global_store_dwordx2 v[54:55], v[20:21], off offset:224
	s_waitcnt vmcnt(8)
	s_cbranch_scc0 .LBB0_779
	v_add_u32_e32 v8, 0xa000, v63
	s_nop 2
	ds_write2_b32 v8, v4, v5 offset0:64 offset1:81
	ds_write2_b32 v8, v6, v7 offset0:98 offset1:115
	s_waitcnt lgkmcnt(0)
	v_mov_b32_e32 v6, 0
	v_mov_b32_e32 v50, 0
	v_mov_b32_e32 v5, 0
	v_mov_b32_e32 v4, 0
	s_and_saveexec_b64 s[16:17], s[40:41]
	s_cbranch_execz .LBB0_782
	v_add_u32_e32 v4, 0xa100, v64
	ds_read2_b32 v[4:5], v4 offset1:1
	s_mov_b32 s4, 0xf149f2ca
	s_waitcnt lgkmcnt(0)
	v_mul_f32_e32 v4, 0xbfb8aa3b, v4
	v_mul_f32_e32 v5, 0xbfb8aa3b, v5
	v_exp_f32_e32 v4, v4
	v_exp_f32_e32 v5, v5
	s_nop 0
	v_pk_add_f32 v[4:5], v[4:5], 1.0 op_sel_hi:[1,0]
	s_nop 0
	v_div_scale_f32 v6, s[0:1], v5, v5, 1.0
	v_rcp_f32_e32 v7, v6
	s_nop 0
	v_fma_f32 v8, -v6, v7, 1.0
	v_fmac_f32_e32 v7, v8, v7
	v_div_scale_f32 v8, vcc, 1.0, v5, 1.0
	v_mul_f32_e32 v9, v8, v7
	v_fma_f32 v10, -v6, v9, v8
	v_fmac_f32_e32 v9, v10, v7
	v_fma_f32 v6, -v6, v9, v8
	v_div_fmas_f32 v6, v6, v7, v9
	v_div_fixup_f32 v17, v6, v5, 1.0
	v_div_scale_f32 v5, s[0:1], v4, v4, 1.0
	v_rcp_f32_e32 v6, v5
	s_nop 0
	v_fma_f32 v7, -v5, v6, 1.0
	v_fmac_f32_e32 v6, v7, v6
	v_div_scale_f32 v7, vcc, 1.0, v4, 1.0
	v_mul_f32_e32 v8, v7, v6
	v_fma_f32 v9, -v5, v8, v7
	v_fmac_f32_e32 v8, v9, v6
	v_fma_f32 v5, -v5, v8, v7
	v_div_fmas_f32 v5, v5, v6, v8
	v_div_fixup_f32 v16, v5, v4, 1.0
	v_mov_b32_e32 v4, v152
	v_mov_b32_e32 v5, v153
	v_mov_b32_e32 v6, v154
	v_mov_b32_e32 v7, v155
	v_mov_b32_e32 v8, v156
	v_mov_b32_e32 v9, v157
	v_mov_b32_e32 v10, v158
	v_mov_b32_e32 v11, v159
	v_mov_b32_e32 v12, v160
	v_mov_b32_e32 v13, v161
	v_mov_b32_e32 v14, v162
	v_mov_b32_e32 v15, v163
	v_mov_b32_e32 v20, v164
	v_mov_b32_e32 v21, v165
	v_mov_b32_e32 v22, v166
	v_mov_b32_e32 v23, v167
	v_pk_add_f32 v[18:19], v[20:21], v[16:17]
	v_add_u32_e32 v20, 0xa108, v64
	ds_read2_b32 v[20:21], v20 offset1:1
	s_waitcnt lgkmcnt(0)
	v_mul_f32_e32 v20, 0xbfb8aa3b, v20
	v_mul_f32_e32 v21, 0xbfb8aa3b, v21
	v_exp_f32_e32 v20, v20
	v_exp_f32_e32 v21, v21
	s_nop 0
	v_pk_add_f32 v[20:21], v[20:21], 1.0 op_sel_hi:[1,0]
	s_nop 0
	v_div_scale_f32 v24, s[0:1], v21, v21, 1.0
	v_rcp_f32_e32 v25, v24
	s_nop 0
	v_fma_f32 v26, -v24, v25, 1.0
	v_fmac_f32_e32 v25, v26, v25
	v_div_scale_f32 v26, vcc, 1.0, v21, 1.0
	v_mul_f32_e32 v27, v26, v25
	v_fma_f32 v28, -v24, v27, v26
	v_fmac_f32_e32 v27, v28, v25
	v_fma_f32 v24, -v24, v27, v26
	v_div_fmas_f32 v24, v24, v25, v27
	v_div_fixup_f32 v21, v24, v21, 1.0
	v_div_scale_f32 v24, s[0:1], v20, v20, 1.0
	v_rcp_f32_e32 v25, v24
	s_nop 0
	v_fma_f32 v26, -v24, v25, 1.0
	v_fmac_f32_e32 v25, v26, v25
	v_div_scale_f32 v26, vcc, 1.0, v20, 1.0
	v_mul_f32_e32 v27, v26, v25
	v_fma_f32 v28, -v24, v27, v26
	v_fmac_f32_e32 v27, v28, v25
	v_fma_f32 v24, -v24, v27, v26
	v_div_fmas_f32 v24, v24, v25, v27
	v_div_fixup_f32 v20, v24, v20, 1.0
	v_add_u32_e32 v24, 0xa110, v64
	ds_read2_b32 v[24:25], v24 offset1:1
	v_pk_add_f32 v[22:23], v[22:23], v[20:21]
	s_waitcnt lgkmcnt(0)
	v_mul_f32_e32 v24, 0xbfb8aa3b, v24
	v_mul_f32_e32 v25, 0xbfb8aa3b, v25
	v_exp_f32_e32 v24, v24
	v_exp_f32_e32 v25, v25
	s_nop 0
	v_pk_add_f32 v[24:25], v[24:25], 1.0 op_sel_hi:[1,0]
	s_nop 0
	v_div_scale_f32 v26, s[0:1], v25, v25, 1.0
	v_rcp_f32_e32 v27, v26
	s_nop 0
	v_fma_f32 v28, -v26, v27, 1.0
	v_fmac_f32_e32 v27, v28, v27
	v_div_scale_f32 v28, vcc, 1.0, v25, 1.0
	v_mul_f32_e32 v29, v28, v27
	v_fma_f32 v30, -v26, v29, v28
	v_fmac_f32_e32 v29, v30, v27
	v_fma_f32 v26, -v26, v29, v28
	v_div_fmas_f32 v26, v26, v27, v29
	v_div_fixup_f32 v25, v26, v25, 1.0
	v_div_scale_f32 v26, s[0:1], v24, v24, 1.0
	v_rcp_f32_e32 v27, v26
	s_nop 0
	v_fma_f32 v28, -v26, v27, 1.0
	v_fmac_f32_e32 v27, v28, v27
	v_div_scale_f32 v28, vcc, 1.0, v24, 1.0
	v_mul_f32_e32 v29, v28, v27
	v_fma_f32 v30, -v26, v29, v28
	v_fmac_f32_e32 v29, v30, v27
	v_fma_f32 v26, -v26, v29, v28
	v_div_fmas_f32 v26, v26, v27, v29
	v_div_fixup_f32 v24, v26, v24, 1.0
	v_add_u32_e32 v26, 0xa118, v64
	ds_read2_b32 v[26:27], v26 offset1:1
	v_pk_add_f32 v[12:13], v[12:13], v[24:25]
	s_waitcnt lgkmcnt(0)
	v_mul_f32_e32 v26, 0xbfb8aa3b, v26
	v_mul_f32_e32 v27, 0xbfb8aa3b, v27
	v_exp_f32_e32 v26, v26
	v_exp_f32_e32 v27, v27
	s_nop 0
	v_pk_add_f32 v[26:27], v[26:27], 1.0 op_sel_hi:[1,0]
	s_nop 0
	v_div_scale_f32 v28, s[0:1], v27, v27, 1.0
	v_rcp_f32_e32 v29, v28
	s_nop 0
	v_fma_f32 v30, -v28, v29, 1.0
	v_fmac_f32_e32 v29, v30, v29
	v_div_scale_f32 v30, vcc, 1.0, v27, 1.0
	v_mul_f32_e32 v31, v30, v29
	v_fma_f32 v46, -v28, v31, v30
	v_fmac_f32_e32 v31, v46, v29
	v_fma_f32 v28, -v28, v31, v30
	v_div_fmas_f32 v28, v28, v29, v31
	v_div_fixup_f32 v27, v28, v27, 1.0
	v_div_scale_f32 v28, s[0:1], v26, v26, 1.0
	v_rcp_f32_e32 v29, v28
	s_nop 0
	v_fma_f32 v30, -v28, v29, 1.0
	v_fmac_f32_e32 v29, v30, v29
	v_div_scale_f32 v30, vcc, 1.0, v26, 1.0
	v_mul_f32_e32 v31, v30, v29
	v_fma_f32 v46, -v28, v31, v30
	v_fmac_f32_e32 v31, v46, v29
	v_fma_f32 v28, -v28, v31, v30
	v_div_fmas_f32 v28, v28, v29, v31
	v_div_fixup_f32 v26, v28, v26, 1.0
	v_add_u32_e32 v28, 0xa120, v64
	ds_read2_b32 v[28:29], v28 offset1:1
	v_pk_add_f32 v[14:15], v[14:15], v[26:27]
	s_waitcnt lgkmcnt(0)
	v_mul_f32_e32 v28, 0xbfb8aa3b, v28
	v_mul_f32_e32 v29, 0xbfb8aa3b, v29
	v_exp_f32_e32 v28, v28
	v_exp_f32_e32 v29, v29
	s_nop 0
	v_pk_add_f32 v[28:29], v[28:29], 1.0 op_sel_hi:[1,0]
	s_nop 0
	v_div_scale_f32 v30, s[0:1], v29, v29, 1.0
	v_rcp_f32_e32 v31, v30
	s_nop 0
	v_fma_f32 v46, -v30, v31, 1.0
	v_fmac_f32_e32 v31, v46, v31
	v_div_scale_f32 v46, vcc, 1.0, v29, 1.0
	v_mul_f32_e32 v47, v46, v31
	v_fma_f32 v48, -v30, v47, v46
	v_fmac_f32_e32 v47, v48, v31
	v_fma_f32 v30, -v30, v47, v46
	v_div_fmas_f32 v30, v30, v31, v47
	v_div_fixup_f32 v29, v30, v29, 1.0
	v_div_scale_f32 v30, s[0:1], v28, v28, 1.0
	v_rcp_f32_e32 v31, v30
	s_nop 0
	v_fma_f32 v46, -v30, v31, 1.0
	v_fmac_f32_e32 v31, v46, v31
	v_div_scale_f32 v46, vcc, 1.0, v28, 1.0
	v_mul_f32_e32 v47, v46, v31
	v_fma_f32 v48, -v30, v47, v46
	v_fmac_f32_e32 v47, v48, v31
	v_fma_f32 v30, -v30, v47, v46
	v_div_fmas_f32 v30, v30, v31, v47
	v_div_fixup_f32 v28, v30, v28, 1.0
	v_add_u32_e32 v30, 0xa128, v64
	ds_read2_b32 v[30:31], v30 offset1:1
	v_pk_add_f32 v[8:9], v[8:9], v[28:29]
	s_waitcnt lgkmcnt(0)
	v_mul_f32_e32 v30, 0xbfb8aa3b, v30
	v_mul_f32_e32 v31, 0xbfb8aa3b, v31
	v_exp_f32_e32 v30, v30
	v_exp_f32_e32 v31, v31
	s_nop 0
	v_pk_add_f32 v[30:31], v[30:31], 1.0 op_sel_hi:[1,0]
	s_nop 0
	v_div_scale_f32 v46, s[0:1], v31, v31, 1.0
	v_rcp_f32_e32 v47, v46
	s_nop 0
	v_fma_f32 v48, -v46, v47, 1.0
	v_fmac_f32_e32 v47, v48, v47
	v_div_scale_f32 v48, vcc, 1.0, v31, 1.0
	v_mul_f32_e32 v49, v48, v47
	v_fma_f32 v51, -v46, v49, v48
	v_fmac_f32_e32 v49, v51, v47
	v_fma_f32 v46, -v46, v49, v48
	v_div_fmas_f32 v46, v46, v47, v49
	v_div_fixup_f32 v31, v46, v31, 1.0
	v_div_scale_f32 v46, s[0:1], v30, v30, 1.0
	v_rcp_f32_e32 v47, v46
	s_nop 0
	v_fma_f32 v48, -v46, v47, 1.0
	v_fmac_f32_e32 v47, v48, v47
	v_div_scale_f32 v48, vcc, 1.0, v30, 1.0
	v_mul_f32_e32 v49, v48, v47
	v_fma_f32 v51, -v46, v49, v48
	v_fmac_f32_e32 v49, v51, v47
	v_fma_f32 v46, -v46, v49, v48
	v_div_fmas_f32 v46, v46, v47, v49
	v_div_fixup_f32 v30, v46, v30, 1.0
	v_add_u32_e32 v46, 0xa130, v64
	ds_read2_b32 v[46:47], v46 offset1:1
	v_pk_add_f32 v[10:11], v[10:11], v[30:31]
	s_waitcnt lgkmcnt(0)
	v_mul_f32_e32 v46, 0xbfb8aa3b, v46
	v_mul_f32_e32 v47, 0xbfb8aa3b, v47
	v_exp_f32_e32 v46, v46
	v_exp_f32_e32 v47, v47
	s_nop 0
	v_pk_add_f32 v[46:47], v[46:47], 1.0 op_sel_hi:[1,0]
	s_nop 0
	v_div_scale_f32 v48, s[0:1], v47, v47, 1.0
	v_rcp_f32_e32 v49, v48
	s_nop 0
	v_fma_f32 v51, -v48, v49, 1.0
	v_fmac_f32_e32 v49, v51, v49
	v_div_scale_f32 v51, vcc, 1.0, v47, 1.0
	v_mul_f32_e32 v52, v51, v49
	v_fma_f32 v53, -v48, v52, v51
	v_fmac_f32_e32 v52, v53, v49
	v_fma_f32 v48, -v48, v52, v51
	v_div_fmas_f32 v48, v48, v49, v52
	v_div_fixup_f32 v47, v48, v47, 1.0
	v_div_scale_f32 v48, s[0:1], v46, v46, 1.0
	v_rcp_f32_e32 v49, v48
	s_nop 0
	v_fma_f32 v51, -v48, v49, 1.0
	v_fmac_f32_e32 v49, v51, v49
	v_div_scale_f32 v51, vcc, 1.0, v46, 1.0
	v_mul_f32_e32 v52, v51, v49
	v_fma_f32 v53, -v48, v52, v51
	v_fmac_f32_e32 v52, v53, v49
	v_fma_f32 v48, -v48, v52, v51
	v_div_fmas_f32 v48, v48, v49, v52
	v_div_fixup_f32 v46, v48, v46, 1.0
	v_add_u32_e32 v48, 0xa138, v64
	ds_read2_b32 v[48:49], v48 offset1:1
	v_pk_add_f32 v[4:5], v[4:5], v[46:47]
	s_waitcnt lgkmcnt(0)
	v_mul_f32_e32 v48, 0xbfb8aa3b, v48
	v_mul_f32_e32 v49, 0xbfb8aa3b, v49
	v_exp_f32_e32 v48, v48
	v_exp_f32_e32 v49, v49
	s_nop 0
	v_pk_add_f32 v[48:49], v[48:49], 1.0 op_sel_hi:[1,0]
	s_nop 0
	v_div_scale_f32 v51, s[0:1], v49, v49, 1.0
	v_rcp_f32_e32 v52, v51
	s_nop 0
	v_fma_f32 v53, -v51, v52, 1.0
	v_fmac_f32_e32 v52, v53, v52
	v_div_scale_f32 v53, vcc, 1.0, v49, 1.0
	v_mul_f32_e32 v54, v53, v52
	v_fma_f32 v55, -v51, v54, v53
	v_fmac_f32_e32 v54, v55, v52
	v_fma_f32 v51, -v51, v54, v53
	v_div_fmas_f32 v51, v51, v52, v54
	v_div_fixup_f32 v49, v51, v49, 1.0
	v_div_scale_f32 v51, s[0:1], v48, v48, 1.0
	v_rcp_f32_e32 v52, v51
	s_nop 0
	v_fma_f32 v53, -v51, v52, 1.0
	v_fmac_f32_e32 v52, v53, v52
	v_div_scale_f32 v53, vcc, 1.0, v48, 1.0
	v_mul_f32_e32 v54, v53, v52
	v_fma_f32 v55, -v51, v54, v53
	v_fmac_f32_e32 v54, v55, v52
	v_fma_f32 v51, -v51, v54, v53
	v_div_fmas_f32 v51, v51, v52, v54
	v_add_f32_e32 v54, v18, v23
	v_add_f32_e32 v55, v19, v22
	v_div_fixup_f32 v48, v51, v48, 1.0
	v_add_f32_e32 v51, v18, v19
	v_pk_add_f32 v[52:53], v[18:19], v[22:23]
	v_max_f32_e32 v54, v54, v55
	v_max3_f32 v51, v51, v52, v54
	v_add_f32_e32 v52, v22, v23
	v_max_f32_e32 v52, v53, v52
	v_max3_f32 v51, v51, v52, s4
	v_add_f32_e32 v54, v12, v13
	v_pk_add_f32 v[52:53], v[12:13], v[14:15]
	v_add_f32_e32 v55, v13, v14
	v_max_f32_e32 v52, v54, v52
	v_add_f32_e32 v54, v12, v15
	v_max_f32_e32 v54, v54, v55
	v_add_f32_e32 v55, v14, v15
	v_max_f32_e32 v53, v53, v55
	v_max3_f32 v52, v52, v54, v53
	v_cmp_gt_f32_e32 vcc, v52, v51
	v_add_f32_e32 v54, v8, v9
	v_add_f32_e32 v55, v9, v10
	v_cndmask_b32_e32 v51, v51, v52, vcc
	v_pk_add_f32 v[52:53], v[8:9], v[10:11]
	v_pk_add_f32 v[6:7], v[6:7], v[48:49]
	v_max_f32_e32 v52, v54, v52
	v_add_f32_e32 v54, v8, v11
	v_max_f32_e32 v54, v54, v55
	v_add_f32_e32 v55, v10, v11
	v_max_f32_e32 v53, v53, v55
	v_max3_f32 v52, v52, v54, v53
	v_cmp_gt_f32_e64 s[0:1], v52, v51
	v_add_f32_e32 v54, v4, v5
	v_add_f32_e32 v55, v5, v6
	v_cndmask_b32_e64 v51, v51, v52, s[0:1]
	v_pk_add_f32 v[52:53], v[4:5], v[6:7]
	s_nop 0
	v_max_f32_e32 v52, v54, v52
	v_add_f32_e32 v54, v4, v7
	v_max_f32_e32 v54, v54, v55
	v_add_f32_e32 v55, v6, v7
	v_max_f32_e32 v53, v53, v55
	v_max3_f32 v52, v52, v54, v53
	v_cmp_ngt_f32_e64 s[2:3], v52, v51
	v_cndmask_b32_e64 v51, 0, 1, vcc
	v_cndmask_b32_e64 v51, v51, 2, s[0:1]
	v_cndmask_b32_e64 v51, 3, v51, s[2:3]
	v_cmp_eq_u32_e32 vcc, 0, v51
	s_nop 1
	v_cndmask_b32_e32 v16, 0, v16, vcc
	v_cndmask_b32_e32 v17, 0, v17, vcc
	v_cndmask_b32_e32 v20, 0, v20, vcc
	v_cndmask_b32_e32 v21, 0, v21, vcc
	v_cndmask_b32_e32 v19, 0, v19, vcc
	v_cndmask_b32_e32 v18, 0, v18, vcc
	v_cndmask_b32_e32 v22, 0, v22, vcc
	v_cndmask_b32_e32 v23, 0, v23, vcc
	v_cmp_eq_u32_e32 vcc, 1, v51
	s_nop 1
	v_cndmask_b32_e32 v21, v21, v27, vcc
	v_cndmask_b32_e32 v20, v20, v26, vcc
	v_cndmask_b32_e32 v17, v17, v25, vcc
	v_cndmask_b32_e32 v16, v16, v24, vcc
	v_cndmask_b32_e32 v15, v23, v15, vcc
	v_cndmask_b32_e32 v14, v22, v14, vcc
	v_cndmask_b32_e32 v12, v18, v12, vcc
	v_cndmask_b32_e32 v13, v19, v13, vcc
	s_and_b64 vcc, s[0:1], s[2:3]
	v_cndmask_b32_e32 v9, v13, v9, vcc
	v_cndmask_b32_e32 v8, v12, v8, vcc
	v_cndmask_b32_e64 v4, v4, v8, s[2:3]
	v_cndmask_b32_e64 v5, v5, v9, s[2:3]
	v_cndmask_b32_e32 v16, v16, v28, vcc
	v_cndmask_b32_e32 v17, v17, v29, vcc
	v_cndmask_b32_e32 v18, v20, v30, vcc
	v_cndmask_b32_e32 v19, v21, v31, vcc
	v_cndmask_b32_e32 v10, v14, v10, vcc
	v_cndmask_b32_e32 v11, v15, v11, vcc
	v_cmp_gt_f32_e32 vcc, v5, v4
	v_cndmask_b32_e64 v6, v6, v10, s[2:3]
	v_cndmask_b32_e64 v7, v7, v11, s[2:3]
	v_cndmask_b32_e32 v9, v4, v5, vcc
	v_cndmask_b32_e64 v8, 0, 1, vcc
	v_cmp_gt_f32_e32 vcc, v6, v9
	v_cndmask_b32_e64 v12, v49, v19, s[2:3]
	v_cndmask_b32_e64 v13, v48, v18, s[2:3]
	v_cndmask_b32_e32 v9, v9, v6, vcc
	v_cndmask_b32_e64 v8, v8, 2, vcc
	v_cmp_ngt_f32_e64 s[0:1], v7, v9
	v_cndmask_b32_e64 v14, v47, v17, s[2:3]
	v_cndmask_b32_e64 v15, v46, v16, s[2:3]
	v_cndmask_b32_e64 v8, 3, v8, s[0:1]
	v_cmp_eq_u32_e64 s[2:3], 0, v8
	v_cmp_nlt_f32_e64 s[4:5], s4, v4
	s_or_b64 s[2:3], s[4:5], s[2:3]
	v_cndmask_b32_e64 v4, v4, v224, s[2:3]
	v_cndmask_b32_e64 v9, 0, -1, s[2:3]
	v_cmp_ne_u32_e64 s[2:3], 1, v8
	v_cmp_gt_f32_e64 s[4:5], v5, v4
	s_and_b64 s[2:3], s[2:3], s[4:5]
	v_cndmask_b32_e64 v4, v4, v5, s[2:3]
	v_cndmask_b32_e64 v9, v9, 1, s[2:3]
	s_and_b64 s[2:3], vcc, s[0:1]
	v_cmp_ngt_f32_e32 vcc, v6, v4
	s_or_b64 vcc, s[2:3], vcc
	s_nop 0
	v_cndmask_b32_e32 v4, v6, v4, vcc
	v_cndmask_b32_e32 v5, 2, v9, vcc
	v_cmp_gt_f32_e32 vcc, v7, v4
	s_and_b64 s[0:1], s[0:1], vcc
	v_cndmask_b32_e64 v4, v5, 3, s[0:1]
	v_min_i32_e32 v5, v8, v4
	v_max_i32_e32 v4, v8, v4
	v_cmp_eq_u32_e32 vcc, 0, v5
	v_subrev_co_u32_e64 v7, s[0:1], 1, v4
	s_nop 0
	v_cndmask_b32_e32 v6, 0, v15, vcc
	v_cndmask_b32_e64 v8, 0, v15, s[0:1]
	v_cmp_eq_u32_e64 s[0:1], 1, v5
	v_cmp_eq_u32_e64 s[2:3], 1, v4
	s_nop 0
	v_cndmask_b32_e64 v6, v6, v14, s[0:1]
	v_cndmask_b32_e64 v8, v8, v14, s[2:3]
	v_cmp_eq_u32_e64 s[2:3], 2, v5
	s_nop 1
	v_cndmask_b32_e64 v6, v6, v13, s[2:3]
	v_cmp_eq_u32_e64 s[2:3], 2, v4
	s_nop 1
	v_cndmask_b32_e64 v8, v8, v13, s[2:3]
	v_cmp_eq_u32_e64 s[2:3], 3, v5
	s_nop 1
	v_cndmask_b32_e64 v5, v6, v12, s[2:3]
	v_cmp_eq_u32_e64 s[2:3], 3, v4
	v_add_u32_e32 v4, 1, v4
	v_cndmask_b32_e64 v4, 5, v4, s[0:1]
	v_cndmask_b32_e64 v8, v8, v12, s[2:3]
	v_add_f32_e32 v6, v5, v8
	v_cndmask_b32_e32 v4, v4, v7, vcc
	v_div_scale_f32 v7, s[0:1], v6, v6, 1.0
	v_rcp_f32_e32 v9, v7
	s_nop 0
	v_fma_f32 v10, -v7, v9, 1.0
	v_fmac_f32_e32 v9, v10, v9
	v_div_scale_f32 v10, vcc, 1.0, v6, 1.0
	v_mul_f32_e32 v11, v10, v9
	v_fma_f32 v12, -v7, v11, v10
	v_fmac_f32_e32 v11, v12, v9
	v_fma_f32 v7, -v7, v11, v10
	v_div_fmas_f32 v7, v7, v9, v11
	v_div_fixup_f32 v7, v7, v6, 1.0
	v_mad_u32_u24 v6, v51, 6, v4
	v_mul_f32_e32 v4, v5, v7
	v_mul_f32_e32 v5, v8, v7
